# T1 projection epilogue: one dispatch on the column tile (PROJ vs US5) and straight-line 16-byte stores instead of per-store saveexec branches with 64-bit multiplies
# speedup vs baseline: 1.0073x; 1.0073x over previous
; __device__ __forceinline__ unsigned cvt_pk_bf16(float lo, float hi) { const f32x2c v = {lo, hi}; const bf16x2c b = __builtin_convertvector(v, bf16x2c); return __builtin_bit_cast(unsigned, b); }
;     __device__ __forceinline__ void operator()(const f32x4 (&acc)[2][2][4][2], const Unit& u, int wr, int wc, int fr, int fq) const {
;         const int row0 = u.pm * BM + wr * 64 + fr, col0 = u.pn * BM + wc * 32 + 8 * fq;
; #pragma unroll
;         for (int ai = 0; ai < 2; ++ai)
; #pragma unroll
;             for (int m = 0; m < 4; ++m) { const size_t row = (size_t)(row0 + ai * HALF + m * 16);
; #pragma unroll
;                 for (int bj = 0; bj < 2; ++bj) { const f32x4 v0 = acc[ai][bj][m][0], v1 = acc[ai][bj][m][1]; const int col = col0 + bj * HALF;
;                     u32x4 w; w.x = cvt_pk_bf16(v0[0], v0[1]); w.y = cvt_pk_bf16(v0[2], v0[3]); w.z = cvt_pk_bf16(v1[0], v1[1]); w.w = cvt_pk_bf16(v1[2], v1[3]);
;                     if (col < DSHIFT) *(u32x4*)(PROJ + row * DSHIFT + col) = w;
;                     else { const int cc = col - DSHIFT; *(u32x4*)(US5 + ((size_t)(cc >> 4) * M + row) * 16 + (cc & 15)) = w; } } }
.LBB0_117:
	v_lshl_add_u32 v150, s18, 8, v139
	s_lshl_b32 s2, s2, 8
	v_mov_b32_e32 v163, v137
	s_cmpk_lt_u32 s2, 0x700
	s_cbranch_scc0 .Lproj_u
	v_mul_u32_u24_e32 v160, s44, v150
	v_mov_b32_e32 v161, v137
	v_or_b32_e32 v162, s2, v155
	v_lshlrev_b32_e32 v162, 1, v162
	v_lshl_add_u64 v[160:161], s[92:93], 0, v[160:161]
	v_lshl_add_u64 v[160:161], v[160:161], 0, v[162:163]
	v_cvt_pk_bf16_f32 v168, v124, v125
	v_cvt_pk_bf16_f32 v169, v126, v127
	v_cvt_pk_bf16_f32 v170, v120, v121
	v_cvt_pk_bf16_f32 v171, v122, v123
	global_store_dwordx4 v[160:161], v[168:171], off
	v_cvt_pk_bf16_f32 v172, v116, v117
	v_cvt_pk_bf16_f32 v173, v118, v119
	v_cvt_pk_bf16_f32 v174, v112, v113
	v_cvt_pk_bf16_f32 v175, v114, v115
	global_store_dwordx4 v[160:161], v[172:175], off offset:256
	s_mov_b64 s[98:99], 0xe000
	v_lshl_add_u64 v[164:165], v[160:161], 0, s[98:99]
	v_cvt_pk_bf16_f32 v168, v108, v109
	v_cvt_pk_bf16_f32 v169, v110, v111
	v_cvt_pk_bf16_f32 v170, v104, v105
	v_cvt_pk_bf16_f32 v171, v106, v107
	global_store_dwordx4 v[164:165], v[168:171], off
	v_cvt_pk_bf16_f32 v172, v100, v101
	v_cvt_pk_bf16_f32 v173, v102, v103
	v_cvt_pk_bf16_f32 v174, v96, v97
	v_cvt_pk_bf16_f32 v175, v98, v99
	global_store_dwordx4 v[164:165], v[172:175], off offset:256
	s_mov_b64 s[98:99], 0x1c000
	v_lshl_add_u64 v[164:165], v[160:161], 0, s[98:99]
	v_cvt_pk_bf16_f32 v168, v92, v93
	v_cvt_pk_bf16_f32 v169, v94, v95
	v_cvt_pk_bf16_f32 v170, v88, v89
	v_cvt_pk_bf16_f32 v171, v90, v91
	global_store_dwordx4 v[164:165], v[168:171], off
	v_cvt_pk_bf16_f32 v172, v84, v85
	v_cvt_pk_bf16_f32 v173, v86, v87
	v_cvt_pk_bf16_f32 v174, v80, v81
	v_cvt_pk_bf16_f32 v175, v82, v83
	global_store_dwordx4 v[164:165], v[172:175], off offset:256
	s_mov_b64 s[98:99], 0x2a000
	v_lshl_add_u64 v[164:165], v[160:161], 0, s[98:99]
	v_cvt_pk_bf16_f32 v168, v76, v77
	v_cvt_pk_bf16_f32 v169, v78, v79
	v_cvt_pk_bf16_f32 v170, v72, v73
	v_cvt_pk_bf16_f32 v171, v74, v75
	global_store_dwordx4 v[164:165], v[168:171], off
	v_cvt_pk_bf16_f32 v172, v68, v69
	v_cvt_pk_bf16_f32 v173, v70, v71
	v_cvt_pk_bf16_f32 v174, v64, v65
	v_cvt_pk_bf16_f32 v175, v66, v67
	global_store_dwordx4 v[164:165], v[172:175], off offset:256
	s_mov_b64 s[98:99], 0x70000
	v_lshl_add_u64 v[164:165], v[160:161], 0, s[98:99]
	v_cvt_pk_bf16_f32 v168, v60, v61
	v_cvt_pk_bf16_f32 v169, v62, v63
	v_cvt_pk_bf16_f32 v170, v56, v57
	v_cvt_pk_bf16_f32 v171, v58, v59
	global_store_dwordx4 v[164:165], v[168:171], off
	v_cvt_pk_bf16_f32 v172, v52, v53
	v_cvt_pk_bf16_f32 v173, v54, v55
	v_cvt_pk_bf16_f32 v174, v48, v49
	v_cvt_pk_bf16_f32 v175, v50, v51
	global_store_dwordx4 v[164:165], v[172:175], off offset:256
	s_mov_b64 s[98:99], 0x7e000
	v_lshl_add_u64 v[164:165], v[160:161], 0, s[98:99]
	v_cvt_pk_bf16_f32 v168, v44, v45
	v_cvt_pk_bf16_f32 v169, v46, v47
	v_cvt_pk_bf16_f32 v170, v40, v41
	v_cvt_pk_bf16_f32 v171, v42, v43
	global_store_dwordx4 v[164:165], v[168:171], off
	v_cvt_pk_bf16_f32 v172, v36, v37
	v_cvt_pk_bf16_f32 v173, v38, v39
	v_cvt_pk_bf16_f32 v174, v32, v33
	v_cvt_pk_bf16_f32 v175, v34, v35
	global_store_dwordx4 v[164:165], v[172:175], off offset:256
	s_mov_b64 s[98:99], 0x8c000
	v_lshl_add_u64 v[164:165], v[160:161], 0, s[98:99]
	v_cvt_pk_bf16_f32 v168, v28, v29
	v_cvt_pk_bf16_f32 v169, v30, v31
	v_cvt_pk_bf16_f32 v170, v24, v25
	v_cvt_pk_bf16_f32 v171, v26, v27
	global_store_dwordx4 v[164:165], v[168:171], off
	v_cvt_pk_bf16_f32 v172, v20, v21
	v_cvt_pk_bf16_f32 v173, v22, v23
	v_cvt_pk_bf16_f32 v174, v16, v17
	v_cvt_pk_bf16_f32 v175, v18, v19
	global_store_dwordx4 v[164:165], v[172:175], off offset:256
	s_mov_b64 s[98:99], 0x9a000
	v_lshl_add_u64 v[164:165], v[160:161], 0, s[98:99]
	v_cvt_pk_bf16_f32 v168, v12, v13
	v_cvt_pk_bf16_f32 v169, v14, v15
	v_cvt_pk_bf16_f32 v170, v8, v9
	v_cvt_pk_bf16_f32 v171, v10, v11
	global_store_dwordx4 v[164:165], v[168:171], off
	v_cvt_pk_bf16_f32 v172, v4, v5
	v_cvt_pk_bf16_f32 v173, v6, v7
	v_cvt_pk_bf16_f32 v174, v0, v1
	v_cvt_pk_bf16_f32 v175, v2, v3
	global_store_dwordx4 v[164:165], v[172:175], off offset:256
	s_branch .Lproj_done
; __device__ __forceinline__ unsigned cvt_pk_bf16(float lo, float hi) { const f32x2c v = {lo, hi}; const bf16x2c b = __builtin_convertvector(v, bf16x2c); return __builtin_bit_cast(unsigned, b); }
;     __device__ __forceinline__ void operator()(const f32x4 (&acc)[2][2][4][2], const Unit& u, int wr, int wc, int fr, int fq) const {
;     ...
;                 for (int bj = 0; bj < 2; ++bj) { const f32x4 v0 = acc[ai][bj][m][0], v1 = acc[ai][bj][m][1]; const int col = col0 + bj * HALF;
;                     u32x4 w; w.x = cvt_pk_bf16(v0[0], v0[1]); w.y = cvt_pk_bf16(v0[2], v0[3]); w.z = cvt_pk_bf16(v1[0], v1[1]); w.w = cvt_pk_bf16(v1[2], v1[3]);
;                     if (col < DSHIFT) *(u32x4*)(PROJ + row * DSHIFT + col) = w;
;                     else { const int cc = col - DSHIFT; *(u32x4*)(US5 + ((size_t)(cc >> 4) * M + row) * 16 + (cc & 15)) = w; } } }
.Lproj_u:
	s_sub_i32 s2, s2, 0x700
	v_or_b32_e32 v162, s2, v155
	v_lshrrev_b32_e32 v162, 4, v162
	v_lshlrev_b64 v[160:161], 21, v[162:163]
	v_lshl_add_u64 v[160:161], s[24:25], 0, v[160:161]
	v_lshlrev_b32_e32 v162, 5, v150
	v_lshl_add_u64 v[160:161], v[160:161], 0, v[162:163]
	v_and_b32_e32 v162, 8, v155
	v_lshlrev_b32_e32 v162, 1, v162
	v_lshl_add_u64 v[160:161], v[160:161], 0, v[162:163]
	s_mov_b64 s[98:99], 0x1000
	v_lshl_add_u64 v[164:165], v[160:161], 0, s[98:99]
	s_mov_b64 s[98:99], 0x1000000
	v_lshl_add_u64 v[166:167], v[160:161], 0, s[98:99]
	v_lshl_add_u64 v[176:177], v[164:165], 0, s[98:99]
	v_cvt_pk_bf16_f32 v168, v124, v125
	v_cvt_pk_bf16_f32 v169, v126, v127
	v_cvt_pk_bf16_f32 v170, v120, v121
	v_cvt_pk_bf16_f32 v171, v122, v123
	global_store_dwordx4 v[160:161], v[168:171], off
	v_cvt_pk_bf16_f32 v172, v116, v117
	v_cvt_pk_bf16_f32 v173, v118, v119
	v_cvt_pk_bf16_f32 v174, v112, v113
	v_cvt_pk_bf16_f32 v175, v114, v115
	global_store_dwordx4 v[166:167], v[172:175], off
	v_cvt_pk_bf16_f32 v168, v108, v109
	v_cvt_pk_bf16_f32 v169, v110, v111
	v_cvt_pk_bf16_f32 v170, v104, v105
	v_cvt_pk_bf16_f32 v171, v106, v107
	global_store_dwordx4 v[160:161], v[168:171], off offset:512
	v_cvt_pk_bf16_f32 v172, v100, v101
	v_cvt_pk_bf16_f32 v173, v102, v103
	v_cvt_pk_bf16_f32 v174, v96, v97
	v_cvt_pk_bf16_f32 v175, v98, v99
	global_store_dwordx4 v[166:167], v[172:175], off offset:512
	v_cvt_pk_bf16_f32 v168, v92, v93
	v_cvt_pk_bf16_f32 v169, v94, v95
	v_cvt_pk_bf16_f32 v170, v88, v89
	v_cvt_pk_bf16_f32 v171, v90, v91
	global_store_dwordx4 v[160:161], v[168:171], off offset:1024
	v_cvt_pk_bf16_f32 v172, v84, v85
	v_cvt_pk_bf16_f32 v173, v86, v87
	v_cvt_pk_bf16_f32 v174, v80, v81
	v_cvt_pk_bf16_f32 v175, v82, v83
	global_store_dwordx4 v[166:167], v[172:175], off offset:1024
	v_cvt_pk_bf16_f32 v168, v76, v77
	v_cvt_pk_bf16_f32 v169, v78, v79
	v_cvt_pk_bf16_f32 v170, v72, v73
	v_cvt_pk_bf16_f32 v171, v74, v75
	global_store_dwordx4 v[160:161], v[168:171], off offset:1536
	v_cvt_pk_bf16_f32 v172, v68, v69
	v_cvt_pk_bf16_f32 v173, v70, v71
	v_cvt_pk_bf16_f32 v174, v64, v65
	v_cvt_pk_bf16_f32 v175, v66, v67
	global_store_dwordx4 v[166:167], v[172:175], off offset:1536
	v_cvt_pk_bf16_f32 v168, v60, v61
	v_cvt_pk_bf16_f32 v169, v62, v63
	v_cvt_pk_bf16_f32 v170, v56, v57
	v_cvt_pk_bf16_f32 v171, v58, v59
	global_store_dwordx4 v[164:165], v[168:171], off
	v_cvt_pk_bf16_f32 v172, v52, v53
	v_cvt_pk_bf16_f32 v173, v54, v55
	v_cvt_pk_bf16_f32 v174, v48, v49
	v_cvt_pk_bf16_f32 v175, v50, v51
	global_store_dwordx4 v[176:177], v[172:175], off
	v_cvt_pk_bf16_f32 v168, v44, v45
	v_cvt_pk_bf16_f32 v169, v46, v47
	v_cvt_pk_bf16_f32 v170, v40, v41
	v_cvt_pk_bf16_f32 v171, v42, v43
	global_store_dwordx4 v[164:165], v[168:171], off offset:512
	v_cvt_pk_bf16_f32 v172, v36, v37
	v_cvt_pk_bf16_f32 v173, v38, v39
	v_cvt_pk_bf16_f32 v174, v32, v33
	v_cvt_pk_bf16_f32 v175, v34, v35
	global_store_dwordx4 v[176:177], v[172:175], off offset:512
	v_cvt_pk_bf16_f32 v168, v28, v29
	v_cvt_pk_bf16_f32 v169, v30, v31
	v_cvt_pk_bf16_f32 v170, v24, v25
	v_cvt_pk_bf16_f32 v171, v26, v27
	global_store_dwordx4 v[164:165], v[168:171], off offset:1024
	v_cvt_pk_bf16_f32 v172, v20, v21
	v_cvt_pk_bf16_f32 v173, v22, v23
	v_cvt_pk_bf16_f32 v174, v16, v17
	v_cvt_pk_bf16_f32 v175, v18, v19
	global_store_dwordx4 v[176:177], v[172:175], off offset:1024
	v_cvt_pk_bf16_f32 v168, v12, v13
	v_cvt_pk_bf16_f32 v169, v14, v15
	v_cvt_pk_bf16_f32 v170, v8, v9
	v_cvt_pk_bf16_f32 v171, v10, v11
	global_store_dwordx4 v[164:165], v[168:171], off offset:1536
	v_cvt_pk_bf16_f32 v172, v4, v5
	v_cvt_pk_bf16_f32 v173, v6, v7
	v_cvt_pk_bf16_f32 v174, v0, v1
	v_cvt_pk_bf16_f32 v175, v2, v3
	global_store_dwordx4 v[176:177], v[172:175], off offset:1536
.Lproj_done:
	s_andn2_b64 vcc, exec, s[0:1]
	s_mov_b64 s[0:1], -1
	s_cbranch_vccnz .LBB0_110
